# pool window loads issued only for the column groups that use the row (exec-masked), on top of w_in 27 tiles + dt routine + interleaved wave index
# baseline (speedup 1.0000x reference)
.LBB0_550:
	s_or_b64 exec, exec, s[0:1]
	s_and_saveexec_b64 s[38:39], s[36:37]
	s_cbranch_execz .LBB0_593
	v_lshlrev_b32_e32 v1, 3, v1
	s_waitcnt vmcnt(7)
	v_mov_b64_e32 v[38:39], v[50:51]
	v_lshl_or_b32 v1, s8, 9, v1
	s_lshl_b32 s3, s10, 9
	s_mov_b64 s[36:37], 0
	v_mov_b64_e32 v[40:41], v[52:53]
	s_mov_b32 s16, 0xffff0000
	s_mov_b32 s17, -1
	s_mov_b32 s18, 0
	s_mov_b32 s19, -1
	s_mov_b32 s20, 0
	s_mov_b32 s21, 0xffff0000
	s_branch .LBB0_554
.LBB0_552:
	s_or_b64 exec, exec, s[0:1]
	s_waitcnt vmcnt(1)
	v_sub_u32_e32 v64, v51, v88
	v_add_u32_e32 v2, v89, v51
	v_max_i32_e32 v65, 0, v64
	s_waitcnt vmcnt(0)
	v_min_i32_e32 v68, v2, v3
	v_add_u32_e32 v2, -8, v51
	v_min_i32_e32 v3, v2, v68
	v_cmp_lt_i32_e64 s[0:1], v2, v65
	v_add_u32_e32 v4, -7, v51
	v_min_i32_e32 v5, v4, v68
	v_cndmask_b32_e64 v2, v3, v65, s[0:1]
	v_cmp_lt_i32_e64 s[0:1], v4, v65
	v_add_u32_e32 v10, -6, v51
	v_min_i32_e32 v11, v10, v68
	v_cndmask_b32_e64 v4, v5, v65, s[0:1]
	v_cmp_lt_i32_e64 s[0:1], v10, v65
	v_add_u32_e32 v12, -5, v51
	v_min_i32_e32 v13, v12, v68
	v_cndmask_b32_e64 v10, v11, v65, s[0:1]
	v_cmp_lt_i32_e64 s[0:1], v12, v65
	v_add_u32_e32 v18, -4, v51
	v_min_i32_e32 v19, v18, v68
	v_cndmask_b32_e64 v12, v13, v65, s[0:1]
	v_cmp_lt_i32_e64 s[0:1], v18, v65
	v_add_u32_e32 v20, -3, v51
	v_min_i32_e32 v21, v20, v68
	v_cndmask_b32_e64 v18, v19, v65, s[0:1]
	v_cmp_lt_i32_e64 s[0:1], v20, v65
	v_add_u32_e32 v26, -2, v51
	v_min_i32_e32 v27, v26, v68
	v_cndmask_b32_e64 v20, v21, v65, s[0:1]
	v_cmp_lt_i32_e64 s[0:1], v26, v65
	v_add_u32_e32 v28, -1, v51
	v_min_i32_e32 v28, v28, v68
	v_cndmask_b32_e64 v26, v27, v65, s[0:1]
	v_cmp_gt_u32_e64 s[0:1], v51, v65
	v_add_u32_e32 v36, 1, v51
	v_min_i32_e32 v37, v36, v68
	v_cndmask_b32_e64 v28, v65, v28, s[0:1]
	v_cmp_gt_i32_e64 s[0:1], v64, v36
	v_add_u32_e32 v42, 2, v51
	v_min_i32_e32 v43, v42, v68
	v_cndmask_b32_e64 v36, v37, v65, s[0:1]
	v_cmp_gt_i32_e64 s[0:1], v64, v42
	v_add_u32_e32 v44, 3, v51
	v_min_i32_e32 v45, v44, v68
	v_cndmask_b32_e64 v42, v43, v65, s[0:1]
	v_cmp_gt_i32_e64 s[0:1], v64, v44
	v_add_u32_e32 v54, 4, v51
	v_min_i32_e32 v55, v54, v68
	v_cndmask_b32_e64 v44, v45, v65, s[0:1]
	v_cmp_gt_i32_e64 s[0:1], v64, v54
	v_add_u32_e32 v56, 5, v51
	v_min_i32_e32 v57, v56, v68
	v_cndmask_b32_e64 v54, v55, v65, s[0:1]
	v_cmp_gt_i32_e64 s[0:1], v64, v56
	v_add_u32_e32 v62, 6, v51
	v_min_i32_e32 v34, v51, v68
	v_cndmask_b32_e64 v56, v57, v65, s[0:1]
	v_min_i32_e32 v63, v62, v68
	v_cmp_gt_i32_e64 s[0:1], v64, v62
	v_add_u32_e32 v51, 7, v51
	v_add_u32_e32 v2, v2, v50
	v_add_u32_e32 v4, v4, v50
	v_add_u32_e32 v10, v10, v50
	v_add_u32_e32 v12, v12, v50
	v_add_u32_e32 v18, v18, v50
	v_add_u32_e32 v20, v20, v50
	v_add_u32_e32 v26, v26, v50
	v_add_u32_e32 v28, v28, v50
	v_add_u32_e32 v34, v34, v50
	v_add_u32_e32 v36, v36, v50
	v_cndmask_b32_e64 v62, v63, v65, s[0:1]
	v_min_i32_e32 v68, v51, v68
	v_cmp_gt_i32_e64 s[0:1], v64, v51
	v_ashrrev_i32_e32 v3, 31, v2
	v_readlane_b32 s4, v252, 8
	v_ashrrev_i32_e32 v5, 31, v4
	v_ashrrev_i32_e32 v11, 31, v10
	v_ashrrev_i32_e32 v13, 31, v12
	v_ashrrev_i32_e32 v19, 31, v18
	v_ashrrev_i32_e32 v21, 31, v20
	v_ashrrev_i32_e32 v27, 31, v26
	v_ashrrev_i32_e32 v29, 31, v28
	v_ashrrev_i32_e32 v35, 31, v34
	v_ashrrev_i32_e32 v37, 31, v36
	v_add_u32_e32 v42, v42, v50
	v_add_u32_e32 v44, v44, v50
	v_add_u32_e32 v54, v54, v50
	v_add_u32_e32 v56, v56, v50
	v_add_u32_e32 v62, v62, v50
	v_cndmask_b32_e64 v51, v68, v65, s[0:1]
	v_lshlrev_b64 v[2:3], 13, v[2:3]
	v_readlane_b32 s5, v252, 9
	v_lshlrev_b64 v[4:5], 13, v[4:5]
	v_lshlrev_b64 v[10:11], 13, v[10:11]
	v_lshlrev_b64 v[12:13], 13, v[12:13]
	v_lshlrev_b64 v[18:19], 13, v[18:19]
	v_lshlrev_b64 v[20:21], 13, v[20:21]
	v_lshlrev_b64 v[26:27], 13, v[26:27]
	v_lshlrev_b64 v[28:29], 13, v[28:29]
	v_lshlrev_b64 v[34:35], 13, v[34:35]
	v_lshlrev_b64 v[36:37], 13, v[36:37]
	v_ashrrev_i32_e32 v43, 31, v42
	v_ashrrev_i32_e32 v45, 31, v44
	v_ashrrev_i32_e32 v55, 31, v54
	v_ashrrev_i32_e32 v57, 31, v56
	v_ashrrev_i32_e32 v63, 31, v62
	v_add_u32_e32 v50, v51, v50
	v_lshl_add_u64 v[2:3], s[4:5], 0, v[2:3]
	v_lshlrev_b32_e32 v52, 1, v66
	v_mov_b32_e32 v53, v67
	v_lshl_add_u64 v[4:5], s[4:5], 0, v[4:5]
	v_lshl_add_u64 v[10:11], s[4:5], 0, v[10:11]
	v_lshl_add_u64 v[12:13], s[4:5], 0, v[12:13]
	v_lshl_add_u64 v[18:19], s[4:5], 0, v[18:19]
	v_lshl_add_u64 v[20:21], s[4:5], 0, v[20:21]
	v_lshl_add_u64 v[26:27], s[4:5], 0, v[26:27]
	v_lshl_add_u64 v[28:29], s[4:5], 0, v[28:29]
	v_lshl_add_u64 v[34:35], s[4:5], 0, v[34:35]
	v_lshl_add_u64 v[36:37], s[4:5], 0, v[36:37]
	v_lshlrev_b64 v[42:43], 13, v[42:43]
	v_lshlrev_b64 v[44:45], 13, v[44:45]
	v_lshlrev_b64 v[54:55], 13, v[54:55]
	v_lshlrev_b64 v[56:57], 13, v[56:57]
	v_lshlrev_b64 v[62:63], 13, v[62:63]
	v_ashrrev_i32_e32 v51, 31, v50
	v_lshl_add_u64 v[2:3], v[2:3], 0, v[52:53]
	v_lshl_add_u64 v[6:7], v[4:5], 0, v[52:53]
	v_lshl_add_u64 v[10:11], v[10:11], 0, v[52:53]
	v_lshl_add_u64 v[14:15], v[12:13], 0, v[52:53]
	v_lshl_add_u64 v[18:19], v[18:19], 0, v[52:53]
	v_lshl_add_u64 v[22:23], v[20:21], 0, v[52:53]
	v_lshl_add_u64 v[26:27], v[26:27], 0, v[52:53]
	v_lshl_add_u64 v[30:31], v[28:29], 0, v[52:53]
	v_lshl_add_u64 v[34:35], v[34:35], 0, v[52:53]
	v_lshl_add_u64 v[36:37], v[36:37], 0, v[52:53]
	v_lshl_add_u64 v[42:43], s[4:5], 0, v[42:43]
	v_lshl_add_u64 v[44:45], s[4:5], 0, v[44:45]
	v_lshl_add_u64 v[54:55], s[4:5], 0, v[54:55]
	v_lshl_add_u64 v[56:57], s[4:5], 0, v[56:57]
	v_lshl_add_u64 v[62:63], s[4:5], 0, v[62:63]
	v_lshlrev_b64 v[50:51], 13, v[50:51]
	s_mov_b64 s[22:23], exec
	s_and_b64 exec, s[22:23], s[20:21]
	global_load_dwordx4 v[2:5], v[2:3], off offset:2560
	s_nop 0
	global_load_dwordx4 v[6:9], v[6:7], off offset:2560
	s_nop 0
	global_load_dwordx4 v[10:13], v[10:11], off offset:2560
	s_nop 0
	global_load_dwordx4 v[14:17], v[14:15], off offset:2560
	s_nop 0
	s_and_b64 exec, s[22:23], s[18:19]
	global_load_dwordx4 v[18:21], v[18:19], off offset:2560
	s_nop 0
	global_load_dwordx4 v[22:25], v[22:23], off offset:2560
	s_nop 0
	s_and_b64 exec, s[22:23], s[16:17]
	global_load_dwordx4 v[26:29], v[26:27], off offset:2560
	s_nop 0
	s_mov_b64 exec, s[22:23]
	global_load_dwordx4 v[30:33], v[30:31], off offset:2560
	s_nop 0
	global_load_dwordx4 v[72:75], v[34:35], off offset:2560
	s_nop 0
	s_and_b64 exec, s[22:23], s[16:17]
	global_load_dwordx4 v[34:37], v[36:37], off offset:2560
	s_and_b64 exec, s[22:23], s[18:19]
	v_lshl_add_u64 v[42:43], v[42:43], 0, v[52:53]
	v_lshl_add_u64 v[46:47], v[44:45], 0, v[52:53]
	v_lshl_add_u64 v[54:55], v[54:55], 0, v[52:53]
	v_lshl_add_u64 v[58:59], v[56:57], 0, v[52:53]
	v_lshl_add_u64 v[62:63], v[62:63], 0, v[52:53]
	v_lshl_add_u64 v[50:51], s[4:5], 0, v[50:51]
	global_load_dwordx4 v[42:45], v[42:43], off offset:2560
	s_nop 0
	global_load_dwordx4 v[46:49], v[46:47], off offset:2560
	s_nop 0
	s_and_b64 exec, s[22:23], s[20:21]
	global_load_dwordx4 v[54:57], v[54:55], off offset:2560
	s_nop 0
	global_load_dwordx4 v[58:61], v[58:59], off offset:2560
	v_lshl_add_u64 v[50:51], v[50:51], 0, v[52:53]
	global_load_dwordx4 v[62:65], v[62:63], off offset:2560
	s_nop 0
	global_load_dwordx4 v[68:71], v[50:51], off offset:2560
	s_mov_b64 exec, s[22:23]
	s_waitcnt vmcnt(7)
	v_mov_b64_e32 v[50:51], v[72:73]
	v_mov_b64_e32 v[52:53], v[74:75]
